# speedup vs baseline: 1.0507x; 1.0480x over previous
.LBB1_25:
	v_lshl_add_u64 v[14:15], v[4:5], 0, v[8:9]
	global_load_dwordx4 v[22:25], v[14:15], off
	v_add_u32_e32 v13, 8, v13
	v_cmp_ge_i32_e32 vcc, v13, v7
	v_lshl_add_u64 v[8:9], v[8:9], 0, s[6:7]
	s_or_b64 s[14:15], vcc, s[14:15]
	s_waitcnt vmcnt(0)
	v_lshlrev_b32_sdwa v19, v12, v22 dst_sel:DWORD dst_unused:UNUSED_PAD src0_sel:DWORD src1_sel:WORD_1
	ds_add_rtn_u32 v20, v19, v11 offset:5664
	ds_read_b32 v15, v19 offset:6688
	v_and_b32_e32 v22, 0xffff, v22
	s_waitcnt lgkmcnt(0)
	v_add3_u32 v20, v20, v10, v15
	v_ashrrev_i32_e32 v21, 31, v20
	v_lshl_add_u64 v[20:21], v[20:21], 4, s[10:11]
	global_store_dwordx4 v[20:21], v[22:25], off
	s_andn2_b64 exec, exec, s[14:15]
	s_cbranch_execnz .LBB1_25
	s_branch .LBB1_22

.LBB1_32:
	s_endpgm
	s_nop 0
	s_nop 0
	s_nop 0
	s_nop 0
	s_nop 0
	s_nop 0
	s_nop 0
	s_nop 0
	s_nop 0
	s_nop 0
	s_nop 0
	s_nop 0
	s_nop 0
	s_nop 0
	s_nop 0
	s_nop 0
	s_nop 0
	s_nop 0
	s_nop 0
	s_nop 0
	s_nop 0
	s_nop 0
	s_nop 0
	s_nop 0
	s_endpgm

.LBB2_48:
	v_readlane_b32 s2, v35, 0
	v_readlane_b32 s3, v35, 16
	s_max_i32 s2, s2, s3
	v_readlane_b32 s3, v35, 32
	v_readlane_b32 s4, v35, 48
	s_nop 0
	v_mov_b32_e32 v2, s3
	v_mov_b32_e32 v3, s4
	v_max3_i32 v2, s2, v2, v3
	s_mov_b32 s2, 3
	v_readfirstlane_b32 s3, v2
	s_add_i32 s3, s3, 3
	s_mul_hi_i32 s3, s3, 0x55555556
	s_lshr_b32 s4, s3, 31
	s_add_i32 s3, s3, s4
	s_mul_i32 s3, s3, 3
	s_setprio 3
	ds_read_b96 v[62:64], v70 offset:768
	s_mov_b32 s21, s44
	s_cmp_gt_i32 s3, 3
	s_cselect_b32 s4, 12, 0
	v_add_u32_e32 v73, s4, v70
	ds_read2_b32 v[78:79], v73 offset0:192 offset1:193
	ds_read_b32 v80, v73 offset:776
	v_mov_b32_e32 v22, 0
	v_mov_b32_e32 v23, v22
	v_mov_b32_e32 v24, v22
	v_mov_b32_e32 v25, v22
	v_mov_b32_e32 v26, v22
	v_mov_b32_e32 v27, v22
	v_mov_b32_e32 v28, v22
	v_mov_b32_e32 v29, v22
	v_mov_b32_e32 v30, v22
	v_mov_b32_e32 v31, v22
	v_mov_b32_e32 v32, v22
	v_mov_b32_e32 v33, v22
	v_mov_b32_e32 v34, v22
	v_mov_b32_e32 v35, v22
	v_mov_b32_e32 v36, v22
	v_mov_b32_e32 v37, v22
	v_mov_b32_e32 v38, v22
	v_mov_b32_e32 v39, v22
	v_mov_b32_e32 v40, v22
	v_mov_b32_e32 v41, v22
	v_mov_b32_e32 v42, v22
	v_mov_b32_e32 v43, v22
	v_mov_b32_e32 v44, v22
	v_mov_b32_e32 v45, v22
	v_mov_b32_e32 v46, v22
	v_mov_b32_e32 v47, v22
	v_mov_b32_e32 v48, v22
	v_mov_b32_e32 v49, v22
	v_mov_b32_e32 v50, v22
	v_mov_b32_e32 v51, v22
	v_mov_b32_e32 v52, v22
	v_mov_b32_e32 v53, v22
	v_mov_b32_e32 v72, v70
	s_mov_b32 s2, 0
	s_waitcnt lgkmcnt(2)
	v_lshl_or_b32 v2, v62, 8, v71
	v_lshl_or_b32 v6, v63, 8, v71
	v_lshl_or_b32 v10, v64, 8, v71
	buffer_load_dwordx4 v[2:5], v2, s[20:23], 0 offen
	buffer_load_dwordx4 v[6:9], v6, s[20:23], 0 offen
	buffer_load_dwordx4 v[10:13], v10, s[20:23], 0 offen
	s_waitcnt lgkmcnt(0)
	v_lshl_or_b32 v14, v78, 8, v71
	v_lshl_or_b32 v18, v79, 8, v71
	v_lshl_or_b32 v74, v80, 8, v71
	buffer_load_dwordx4 v[14:17], v14, s[20:23], 0 offen
	buffer_load_dwordx4 v[18:21], v18, s[20:23], 0 offen
	buffer_load_dwordx4 v[74:77], v74, s[20:23], 0 offen
.Ll1g_loopE:
	s_add_i32 s5, s2, 6
	s_cmp_ge_i32 s5, s3
	s_cbranch_scc1 .Ll1g_tailE
	ds_read_b128 v[86:89], v72
	ds_read_b128 v[90:93], v72 offset:16
	s_lshl_b32 s4, s5, 2
	v_add_u32_e32 v73, s4, v70
	ds_read2_b32 v[62:63], v73 offset0:192 offset1:193
	ds_read_b32 v64, v73 offset:776
	s_waitcnt vmcnt(3)
	v_cvt_f32_f16_sdwa v55, v2 dst_sel:DWORD dst_unused:UNUSED_PAD src0_sel:WORD_1
	v_cvt_f32_f16_e32 v54, v2
	v_cvt_f32_f16_sdwa v57, v3 dst_sel:DWORD dst_unused:UNUSED_PAD src0_sel:WORD_1
	v_cvt_f32_f16_e32 v56, v3
	v_cvt_f32_f16_sdwa v59, v4 dst_sel:DWORD dst_unused:UNUSED_PAD src0_sel:WORD_1
	v_cvt_f32_f16_e32 v58, v4
	v_cvt_f32_f16_sdwa v61, v5 dst_sel:DWORD dst_unused:UNUSED_PAD src0_sel:WORD_1
	v_cvt_f32_f16_e32 v60, v5
	v_cvt_f32_f16_sdwa v79, v6 dst_sel:DWORD dst_unused:UNUSED_PAD src0_sel:WORD_1
	v_cvt_f32_f16_e32 v78, v6
	v_cvt_f32_f16_sdwa v81, v7 dst_sel:DWORD dst_unused:UNUSED_PAD src0_sel:WORD_1
	v_cvt_f32_f16_e32 v80, v7
	v_cvt_f32_f16_sdwa v83, v8 dst_sel:DWORD dst_unused:UNUSED_PAD src0_sel:WORD_1
	v_cvt_f32_f16_e32 v82, v8
	v_cvt_f32_f16_sdwa v85, v9 dst_sel:DWORD dst_unused:UNUSED_PAD src0_sel:WORD_1
	v_cvt_f32_f16_e32 v84, v9
	s_waitcnt lgkmcnt(3)
	v_pk_fma_f32 v[22:23], v[86:87], v[54:55], v[22:23] op_sel_hi:[0,1,1]
	v_pk_fma_f32 v[30:31], v[86:87], v[54:55], v[30:31] op_sel:[1,0,0]
	v_pk_fma_f32 v[38:39], v[88:89], v[54:55], v[38:39] op_sel_hi:[0,1,1]
	v_pk_fma_f32 v[46:47], v[88:89], v[54:55], v[46:47] op_sel:[1,0,0]
	v_pk_fma_f32 v[24:25], v[86:87], v[56:57], v[24:25] op_sel_hi:[0,1,1]
	v_pk_fma_f32 v[32:33], v[86:87], v[56:57], v[32:33] op_sel:[1,0,0]
	v_pk_fma_f32 v[40:41], v[88:89], v[56:57], v[40:41] op_sel_hi:[0,1,1]
	v_pk_fma_f32 v[48:49], v[88:89], v[56:57], v[48:49] op_sel:[1,0,0]
	v_pk_fma_f32 v[26:27], v[86:87], v[58:59], v[26:27] op_sel_hi:[0,1,1]
	v_pk_fma_f32 v[34:35], v[86:87], v[58:59], v[34:35] op_sel:[1,0,0]
	v_pk_fma_f32 v[42:43], v[88:89], v[58:59], v[42:43] op_sel_hi:[0,1,1]
	v_pk_fma_f32 v[50:51], v[88:89], v[58:59], v[50:51] op_sel:[1,0,0]
	v_pk_fma_f32 v[28:29], v[86:87], v[60:61], v[28:29] op_sel_hi:[0,1,1]
	v_pk_fma_f32 v[36:37], v[86:87], v[60:61], v[36:37] op_sel:[1,0,0]
	v_pk_fma_f32 v[44:45], v[88:89], v[60:61], v[44:45] op_sel_hi:[0,1,1]
	v_pk_fma_f32 v[52:53], v[88:89], v[60:61], v[52:53] op_sel:[1,0,0]
	ds_read_b128 v[86:89], v72 offset:32
	v_cvt_f32_f16_sdwa v55, v10 dst_sel:DWORD dst_unused:UNUSED_PAD src0_sel:WORD_1
	v_cvt_f32_f16_e32 v54, v10
	v_cvt_f32_f16_sdwa v57, v11 dst_sel:DWORD dst_unused:UNUSED_PAD src0_sel:WORD_1
	v_cvt_f32_f16_e32 v56, v11
	v_cvt_f32_f16_sdwa v59, v12 dst_sel:DWORD dst_unused:UNUSED_PAD src0_sel:WORD_1
	v_cvt_f32_f16_e32 v58, v12
	v_cvt_f32_f16_sdwa v61, v13 dst_sel:DWORD dst_unused:UNUSED_PAD src0_sel:WORD_1
	v_cvt_f32_f16_e32 v60, v13
	s_waitcnt lgkmcnt(1)
	v_lshl_or_b32 v2, v62, 8, v71
	v_lshl_or_b32 v6, v63, 8, v71
	v_lshl_or_b32 v10, v64, 8, v71
	buffer_load_dwordx4 v[2:5], v2, s[20:23], 0 offen
	buffer_load_dwordx4 v[6:9], v6, s[20:23], 0 offen
	buffer_load_dwordx4 v[10:13], v10, s[20:23], 0 offen
	v_pk_fma_f32 v[22:23], v[90:91], v[78:79], v[22:23] op_sel_hi:[0,1,1]
	v_pk_fma_f32 v[30:31], v[90:91], v[78:79], v[30:31] op_sel:[1,0,0]
	v_pk_fma_f32 v[38:39], v[92:93], v[78:79], v[38:39] op_sel_hi:[0,1,1]
	v_pk_fma_f32 v[46:47], v[92:93], v[78:79], v[46:47] op_sel:[1,0,0]
	v_pk_fma_f32 v[24:25], v[90:91], v[80:81], v[24:25] op_sel_hi:[0,1,1]
	v_pk_fma_f32 v[32:33], v[90:91], v[80:81], v[32:33] op_sel:[1,0,0]
	v_pk_fma_f32 v[40:41], v[92:93], v[80:81], v[40:41] op_sel_hi:[0,1,1]
	v_pk_fma_f32 v[48:49], v[92:93], v[80:81], v[48:49] op_sel:[1,0,0]
	v_pk_fma_f32 v[26:27], v[90:91], v[82:83], v[26:27] op_sel_hi:[0,1,1]
	v_pk_fma_f32 v[34:35], v[90:91], v[82:83], v[34:35] op_sel:[1,0,0]
	v_pk_fma_f32 v[42:43], v[92:93], v[82:83], v[42:43] op_sel_hi:[0,1,1]
	v_pk_fma_f32 v[50:51], v[92:93], v[82:83], v[50:51] op_sel:[1,0,0]
	v_pk_fma_f32 v[28:29], v[90:91], v[84:85], v[28:29] op_sel_hi:[0,1,1]
	v_pk_fma_f32 v[36:37], v[90:91], v[84:85], v[36:37] op_sel:[1,0,0]
	v_pk_fma_f32 v[44:45], v[92:93], v[84:85], v[44:45] op_sel_hi:[0,1,1]
	v_pk_fma_f32 v[52:53], v[92:93], v[84:85], v[52:53] op_sel:[1,0,0]
	s_waitcnt lgkmcnt(0)
	v_pk_fma_f32 v[22:23], v[86:87], v[54:55], v[22:23] op_sel_hi:[0,1,1]
	v_pk_fma_f32 v[30:31], v[86:87], v[54:55], v[30:31] op_sel:[1,0,0]
	v_pk_fma_f32 v[38:39], v[88:89], v[54:55], v[38:39] op_sel_hi:[0,1,1]
	v_pk_fma_f32 v[46:47], v[88:89], v[54:55], v[46:47] op_sel:[1,0,0]
	v_pk_fma_f32 v[24:25], v[86:87], v[56:57], v[24:25] op_sel_hi:[0,1,1]
	v_pk_fma_f32 v[32:33], v[86:87], v[56:57], v[32:33] op_sel:[1,0,0]
	v_pk_fma_f32 v[40:41], v[88:89], v[56:57], v[40:41] op_sel_hi:[0,1,1]
	v_pk_fma_f32 v[48:49], v[88:89], v[56:57], v[48:49] op_sel:[1,0,0]
	v_pk_fma_f32 v[26:27], v[86:87], v[58:59], v[26:27] op_sel_hi:[0,1,1]
	v_pk_fma_f32 v[34:35], v[86:87], v[58:59], v[34:35] op_sel:[1,0,0]
	v_pk_fma_f32 v[42:43], v[88:89], v[58:59], v[42:43] op_sel_hi:[0,1,1]
	v_pk_fma_f32 v[50:51], v[88:89], v[58:59], v[50:51] op_sel:[1,0,0]
	v_pk_fma_f32 v[28:29], v[86:87], v[60:61], v[28:29] op_sel_hi:[0,1,1]
	v_pk_fma_f32 v[36:37], v[86:87], v[60:61], v[36:37] op_sel:[1,0,0]
	v_pk_fma_f32 v[44:45], v[88:89], v[60:61], v[44:45] op_sel_hi:[0,1,1]
	v_pk_fma_f32 v[52:53], v[88:89], v[60:61], v[52:53] op_sel:[1,0,0]
	v_add_u32_e32 v72, 48, v72
	s_add_i32 s2, s2, 3
.Ll1g_loopO:
	s_add_i32 s5, s2, 6
	s_cmp_ge_i32 s5, s3
	s_cbranch_scc1 .Ll1g_tailO
	ds_read_b128 v[86:89], v72
	ds_read_b128 v[90:93], v72 offset:16
	s_lshl_b32 s4, s5, 2
	v_add_u32_e32 v73, s4, v70
	ds_read2_b32 v[62:63], v73 offset0:192 offset1:193
	ds_read_b32 v64, v73 offset:776
	s_waitcnt vmcnt(3)
	v_cvt_f32_f16_sdwa v55, v14 dst_sel:DWORD dst_unused:UNUSED_PAD src0_sel:WORD_1
	v_cvt_f32_f16_e32 v54, v14
	v_cvt_f32_f16_sdwa v57, v15 dst_sel:DWORD dst_unused:UNUSED_PAD src0_sel:WORD_1
	v_cvt_f32_f16_e32 v56, v15
	v_cvt_f32_f16_sdwa v59, v16 dst_sel:DWORD dst_unused:UNUSED_PAD src0_sel:WORD_1
	v_cvt_f32_f16_e32 v58, v16
	v_cvt_f32_f16_sdwa v61, v17 dst_sel:DWORD dst_unused:UNUSED_PAD src0_sel:WORD_1
	v_cvt_f32_f16_e32 v60, v17
	v_cvt_f32_f16_sdwa v79, v18 dst_sel:DWORD dst_unused:UNUSED_PAD src0_sel:WORD_1
	v_cvt_f32_f16_e32 v78, v18
	v_cvt_f32_f16_sdwa v81, v19 dst_sel:DWORD dst_unused:UNUSED_PAD src0_sel:WORD_1
	v_cvt_f32_f16_e32 v80, v19
	v_cvt_f32_f16_sdwa v83, v20 dst_sel:DWORD dst_unused:UNUSED_PAD src0_sel:WORD_1
	v_cvt_f32_f16_e32 v82, v20
	v_cvt_f32_f16_sdwa v85, v21 dst_sel:DWORD dst_unused:UNUSED_PAD src0_sel:WORD_1
	v_cvt_f32_f16_e32 v84, v21
	s_waitcnt lgkmcnt(3)
	v_pk_fma_f32 v[22:23], v[86:87], v[54:55], v[22:23] op_sel_hi:[0,1,1]
	v_pk_fma_f32 v[30:31], v[86:87], v[54:55], v[30:31] op_sel:[1,0,0]
	v_pk_fma_f32 v[38:39], v[88:89], v[54:55], v[38:39] op_sel_hi:[0,1,1]
	v_pk_fma_f32 v[46:47], v[88:89], v[54:55], v[46:47] op_sel:[1,0,0]
	v_pk_fma_f32 v[24:25], v[86:87], v[56:57], v[24:25] op_sel_hi:[0,1,1]
	v_pk_fma_f32 v[32:33], v[86:87], v[56:57], v[32:33] op_sel:[1,0,0]
	v_pk_fma_f32 v[40:41], v[88:89], v[56:57], v[40:41] op_sel_hi:[0,1,1]
	v_pk_fma_f32 v[48:49], v[88:89], v[56:57], v[48:49] op_sel:[1,0,0]
	v_pk_fma_f32 v[26:27], v[86:87], v[58:59], v[26:27] op_sel_hi:[0,1,1]
	v_pk_fma_f32 v[34:35], v[86:87], v[58:59], v[34:35] op_sel:[1,0,0]
	v_pk_fma_f32 v[42:43], v[88:89], v[58:59], v[42:43] op_sel_hi:[0,1,1]
	v_pk_fma_f32 v[50:51], v[88:89], v[58:59], v[50:51] op_sel:[1,0,0]
	v_pk_fma_f32 v[28:29], v[86:87], v[60:61], v[28:29] op_sel_hi:[0,1,1]
	v_pk_fma_f32 v[36:37], v[86:87], v[60:61], v[36:37] op_sel:[1,0,0]
	v_pk_fma_f32 v[44:45], v[88:89], v[60:61], v[44:45] op_sel_hi:[0,1,1]
	v_pk_fma_f32 v[52:53], v[88:89], v[60:61], v[52:53] op_sel:[1,0,0]
	ds_read_b128 v[86:89], v72 offset:32
	v_cvt_f32_f16_sdwa v55, v74 dst_sel:DWORD dst_unused:UNUSED_PAD src0_sel:WORD_1
	v_cvt_f32_f16_e32 v54, v74
	v_cvt_f32_f16_sdwa v57, v75 dst_sel:DWORD dst_unused:UNUSED_PAD src0_sel:WORD_1
	v_cvt_f32_f16_e32 v56, v75
	v_cvt_f32_f16_sdwa v59, v76 dst_sel:DWORD dst_unused:UNUSED_PAD src0_sel:WORD_1
	v_cvt_f32_f16_e32 v58, v76
	v_cvt_f32_f16_sdwa v61, v77 dst_sel:DWORD dst_unused:UNUSED_PAD src0_sel:WORD_1
	v_cvt_f32_f16_e32 v60, v77
	s_waitcnt lgkmcnt(1)
	v_lshl_or_b32 v14, v62, 8, v71
	v_lshl_or_b32 v18, v63, 8, v71
	v_lshl_or_b32 v74, v64, 8, v71
	buffer_load_dwordx4 v[14:17], v14, s[20:23], 0 offen
	buffer_load_dwordx4 v[18:21], v18, s[20:23], 0 offen
	buffer_load_dwordx4 v[74:77], v74, s[20:23], 0 offen
	v_pk_fma_f32 v[22:23], v[90:91], v[78:79], v[22:23] op_sel_hi:[0,1,1]
	v_pk_fma_f32 v[30:31], v[90:91], v[78:79], v[30:31] op_sel:[1,0,0]
	v_pk_fma_f32 v[38:39], v[92:93], v[78:79], v[38:39] op_sel_hi:[0,1,1]
	v_pk_fma_f32 v[46:47], v[92:93], v[78:79], v[46:47] op_sel:[1,0,0]
	v_pk_fma_f32 v[24:25], v[90:91], v[80:81], v[24:25] op_sel_hi:[0,1,1]
	v_pk_fma_f32 v[32:33], v[90:91], v[80:81], v[32:33] op_sel:[1,0,0]
	v_pk_fma_f32 v[40:41], v[92:93], v[80:81], v[40:41] op_sel_hi:[0,1,1]
	v_pk_fma_f32 v[48:49], v[92:93], v[80:81], v[48:49] op_sel:[1,0,0]
	v_pk_fma_f32 v[26:27], v[90:91], v[82:83], v[26:27] op_sel_hi:[0,1,1]
	v_pk_fma_f32 v[34:35], v[90:91], v[82:83], v[34:35] op_sel:[1,0,0]
	v_pk_fma_f32 v[42:43], v[92:93], v[82:83], v[42:43] op_sel_hi:[0,1,1]
	v_pk_fma_f32 v[50:51], v[92:93], v[82:83], v[50:51] op_sel:[1,0,0]
	v_pk_fma_f32 v[28:29], v[90:91], v[84:85], v[28:29] op_sel_hi:[0,1,1]
	v_pk_fma_f32 v[36:37], v[90:91], v[84:85], v[36:37] op_sel:[1,0,0]
	v_pk_fma_f32 v[44:45], v[92:93], v[84:85], v[44:45] op_sel_hi:[0,1,1]
	v_pk_fma_f32 v[52:53], v[92:93], v[84:85], v[52:53] op_sel:[1,0,0]
	s_waitcnt lgkmcnt(0)
	v_pk_fma_f32 v[22:23], v[86:87], v[54:55], v[22:23] op_sel_hi:[0,1,1]
	v_pk_fma_f32 v[30:31], v[86:87], v[54:55], v[30:31] op_sel:[1,0,0]
	v_pk_fma_f32 v[38:39], v[88:89], v[54:55], v[38:39] op_sel_hi:[0,1,1]
	v_pk_fma_f32 v[46:47], v[88:89], v[54:55], v[46:47] op_sel:[1,0,0]
	v_pk_fma_f32 v[24:25], v[86:87], v[56:57], v[24:25] op_sel_hi:[0,1,1]
	v_pk_fma_f32 v[32:33], v[86:87], v[56:57], v[32:33] op_sel:[1,0,0]
	v_pk_fma_f32 v[40:41], v[88:89], v[56:57], v[40:41] op_sel_hi:[0,1,1]
	v_pk_fma_f32 v[48:49], v[88:89], v[56:57], v[48:49] op_sel:[1,0,0]
	v_pk_fma_f32 v[26:27], v[86:87], v[58:59], v[26:27] op_sel_hi:[0,1,1]
	v_pk_fma_f32 v[34:35], v[86:87], v[58:59], v[34:35] op_sel:[1,0,0]
	v_pk_fma_f32 v[42:43], v[88:89], v[58:59], v[42:43] op_sel_hi:[0,1,1]
	v_pk_fma_f32 v[50:51], v[88:89], v[58:59], v[50:51] op_sel:[1,0,0]
	v_pk_fma_f32 v[28:29], v[86:87], v[60:61], v[28:29] op_sel_hi:[0,1,1]
	v_pk_fma_f32 v[36:37], v[86:87], v[60:61], v[36:37] op_sel:[1,0,0]
	v_pk_fma_f32 v[44:45], v[88:89], v[60:61], v[44:45] op_sel_hi:[0,1,1]
	v_pk_fma_f32 v[52:53], v[88:89], v[60:61], v[52:53] op_sel:[1,0,0]
	v_add_u32_e32 v72, 48, v72
	s_add_i32 s2, s2, 3
	s_branch .Ll1g_loopE
.Ll1g_tailE:
	s_add_i32 s5, s2, 3
	s_cmp_ge_i32 s5, s3
	s_cbranch_scc1 .Ll1g_lastE
	ds_read_b128 v[86:89], v72
	ds_read_b128 v[90:93], v72 offset:16
	s_waitcnt vmcnt(3)
	v_cvt_f32_f16_sdwa v55, v2 dst_sel:DWORD dst_unused:UNUSED_PAD src0_sel:WORD_1
	v_cvt_f32_f16_e32 v54, v2
	v_cvt_f32_f16_sdwa v57, v3 dst_sel:DWORD dst_unused:UNUSED_PAD src0_sel:WORD_1
	v_cvt_f32_f16_e32 v56, v3
	v_cvt_f32_f16_sdwa v59, v4 dst_sel:DWORD dst_unused:UNUSED_PAD src0_sel:WORD_1
	v_cvt_f32_f16_e32 v58, v4
	v_cvt_f32_f16_sdwa v61, v5 dst_sel:DWORD dst_unused:UNUSED_PAD src0_sel:WORD_1
	v_cvt_f32_f16_e32 v60, v5
	v_cvt_f32_f16_sdwa v79, v6 dst_sel:DWORD dst_unused:UNUSED_PAD src0_sel:WORD_1
	v_cvt_f32_f16_e32 v78, v6
	v_cvt_f32_f16_sdwa v81, v7 dst_sel:DWORD dst_unused:UNUSED_PAD src0_sel:WORD_1
	v_cvt_f32_f16_e32 v80, v7
	v_cvt_f32_f16_sdwa v83, v8 dst_sel:DWORD dst_unused:UNUSED_PAD src0_sel:WORD_1
	v_cvt_f32_f16_e32 v82, v8
	v_cvt_f32_f16_sdwa v85, v9 dst_sel:DWORD dst_unused:UNUSED_PAD src0_sel:WORD_1
	v_cvt_f32_f16_e32 v84, v9
	s_waitcnt lgkmcnt(1)
	v_pk_fma_f32 v[22:23], v[86:87], v[54:55], v[22:23] op_sel_hi:[0,1,1]
	v_pk_fma_f32 v[30:31], v[86:87], v[54:55], v[30:31] op_sel:[1,0,0]
	v_pk_fma_f32 v[38:39], v[88:89], v[54:55], v[38:39] op_sel_hi:[0,1,1]
	v_pk_fma_f32 v[46:47], v[88:89], v[54:55], v[46:47] op_sel:[1,0,0]
	v_pk_fma_f32 v[24:25], v[86:87], v[56:57], v[24:25] op_sel_hi:[0,1,1]
	v_pk_fma_f32 v[32:33], v[86:87], v[56:57], v[32:33] op_sel:[1,0,0]
	v_pk_fma_f32 v[40:41], v[88:89], v[56:57], v[40:41] op_sel_hi:[0,1,1]
	v_pk_fma_f32 v[48:49], v[88:89], v[56:57], v[48:49] op_sel:[1,0,0]
	v_pk_fma_f32 v[26:27], v[86:87], v[58:59], v[26:27] op_sel_hi:[0,1,1]
	v_pk_fma_f32 v[34:35], v[86:87], v[58:59], v[34:35] op_sel:[1,0,0]
	v_pk_fma_f32 v[42:43], v[88:89], v[58:59], v[42:43] op_sel_hi:[0,1,1]
	v_pk_fma_f32 v[50:51], v[88:89], v[58:59], v[50:51] op_sel:[1,0,0]
	v_pk_fma_f32 v[28:29], v[86:87], v[60:61], v[28:29] op_sel_hi:[0,1,1]
	v_pk_fma_f32 v[36:37], v[86:87], v[60:61], v[36:37] op_sel:[1,0,0]
	v_pk_fma_f32 v[44:45], v[88:89], v[60:61], v[44:45] op_sel_hi:[0,1,1]
	v_pk_fma_f32 v[52:53], v[88:89], v[60:61], v[52:53] op_sel:[1,0,0]
	ds_read_b128 v[86:89], v72 offset:32
	v_cvt_f32_f16_sdwa v55, v10 dst_sel:DWORD dst_unused:UNUSED_PAD src0_sel:WORD_1
	v_cvt_f32_f16_e32 v54, v10
	v_cvt_f32_f16_sdwa v57, v11 dst_sel:DWORD dst_unused:UNUSED_PAD src0_sel:WORD_1
	v_cvt_f32_f16_e32 v56, v11
	v_cvt_f32_f16_sdwa v59, v12 dst_sel:DWORD dst_unused:UNUSED_PAD src0_sel:WORD_1
	v_cvt_f32_f16_e32 v58, v12
	v_cvt_f32_f16_sdwa v61, v13 dst_sel:DWORD dst_unused:UNUSED_PAD src0_sel:WORD_1
	v_cvt_f32_f16_e32 v60, v13
	s_waitcnt lgkmcnt(1)
	v_pk_fma_f32 v[22:23], v[90:91], v[78:79], v[22:23] op_sel_hi:[0,1,1]
	v_pk_fma_f32 v[30:31], v[90:91], v[78:79], v[30:31] op_sel:[1,0,0]
	v_pk_fma_f32 v[38:39], v[92:93], v[78:79], v[38:39] op_sel_hi:[0,1,1]
	v_pk_fma_f32 v[46:47], v[92:93], v[78:79], v[46:47] op_sel:[1,0,0]
	v_pk_fma_f32 v[24:25], v[90:91], v[80:81], v[24:25] op_sel_hi:[0,1,1]
	v_pk_fma_f32 v[32:33], v[90:91], v[80:81], v[32:33] op_sel:[1,0,0]
	v_pk_fma_f32 v[40:41], v[92:93], v[80:81], v[40:41] op_sel_hi:[0,1,1]
	v_pk_fma_f32 v[48:49], v[92:93], v[80:81], v[48:49] op_sel:[1,0,0]
	v_pk_fma_f32 v[26:27], v[90:91], v[82:83], v[26:27] op_sel_hi:[0,1,1]
	v_pk_fma_f32 v[34:35], v[90:91], v[82:83], v[34:35] op_sel:[1,0,0]
	v_pk_fma_f32 v[42:43], v[92:93], v[82:83], v[42:43] op_sel_hi:[0,1,1]
	v_pk_fma_f32 v[50:51], v[92:93], v[82:83], v[50:51] op_sel:[1,0,0]
	v_pk_fma_f32 v[28:29], v[90:91], v[84:85], v[28:29] op_sel_hi:[0,1,1]
	v_pk_fma_f32 v[36:37], v[90:91], v[84:85], v[36:37] op_sel:[1,0,0]
	v_pk_fma_f32 v[44:45], v[92:93], v[84:85], v[44:45] op_sel_hi:[0,1,1]
	v_pk_fma_f32 v[52:53], v[92:93], v[84:85], v[52:53] op_sel:[1,0,0]
	s_waitcnt lgkmcnt(0)
	v_pk_fma_f32 v[22:23], v[86:87], v[54:55], v[22:23] op_sel_hi:[0,1,1]
	v_pk_fma_f32 v[30:31], v[86:87], v[54:55], v[30:31] op_sel:[1,0,0]
	v_pk_fma_f32 v[38:39], v[88:89], v[54:55], v[38:39] op_sel_hi:[0,1,1]
	v_pk_fma_f32 v[46:47], v[88:89], v[54:55], v[46:47] op_sel:[1,0,0]
	v_pk_fma_f32 v[24:25], v[86:87], v[56:57], v[24:25] op_sel_hi:[0,1,1]
	v_pk_fma_f32 v[32:33], v[86:87], v[56:57], v[32:33] op_sel:[1,0,0]
	v_pk_fma_f32 v[40:41], v[88:89], v[56:57], v[40:41] op_sel_hi:[0,1,1]
	v_pk_fma_f32 v[48:49], v[88:89], v[56:57], v[48:49] op_sel:[1,0,0]
	v_pk_fma_f32 v[26:27], v[86:87], v[58:59], v[26:27] op_sel_hi:[0,1,1]
	v_pk_fma_f32 v[34:35], v[86:87], v[58:59], v[34:35] op_sel:[1,0,0]
	v_pk_fma_f32 v[42:43], v[88:89], v[58:59], v[42:43] op_sel_hi:[0,1,1]
	v_pk_fma_f32 v[50:51], v[88:89], v[58:59], v[50:51] op_sel:[1,0,0]
	v_pk_fma_f32 v[28:29], v[86:87], v[60:61], v[28:29] op_sel_hi:[0,1,1]
	v_pk_fma_f32 v[36:37], v[86:87], v[60:61], v[36:37] op_sel:[1,0,0]
	v_pk_fma_f32 v[44:45], v[88:89], v[60:61], v[44:45] op_sel_hi:[0,1,1]
	v_pk_fma_f32 v[52:53], v[88:89], v[60:61], v[52:53] op_sel:[1,0,0]
	v_add_u32_e32 v72, 48, v72
	s_add_i32 s2, s2, 3
	ds_read_b128 v[86:89], v72
	ds_read_b128 v[90:93], v72 offset:16
	s_waitcnt vmcnt(0)
	v_cvt_f32_f16_sdwa v55, v14 dst_sel:DWORD dst_unused:UNUSED_PAD src0_sel:WORD_1
	v_cvt_f32_f16_e32 v54, v14
	v_cvt_f32_f16_sdwa v57, v15 dst_sel:DWORD dst_unused:UNUSED_PAD src0_sel:WORD_1
	v_cvt_f32_f16_e32 v56, v15
	v_cvt_f32_f16_sdwa v59, v16 dst_sel:DWORD dst_unused:UNUSED_PAD src0_sel:WORD_1
	v_cvt_f32_f16_e32 v58, v16
	v_cvt_f32_f16_sdwa v61, v17 dst_sel:DWORD dst_unused:UNUSED_PAD src0_sel:WORD_1
	v_cvt_f32_f16_e32 v60, v17
	v_cvt_f32_f16_sdwa v79, v18 dst_sel:DWORD dst_unused:UNUSED_PAD src0_sel:WORD_1
	v_cvt_f32_f16_e32 v78, v18
	v_cvt_f32_f16_sdwa v81, v19 dst_sel:DWORD dst_unused:UNUSED_PAD src0_sel:WORD_1
	v_cvt_f32_f16_e32 v80, v19
	v_cvt_f32_f16_sdwa v83, v20 dst_sel:DWORD dst_unused:UNUSED_PAD src0_sel:WORD_1
	v_cvt_f32_f16_e32 v82, v20
	v_cvt_f32_f16_sdwa v85, v21 dst_sel:DWORD dst_unused:UNUSED_PAD src0_sel:WORD_1
	v_cvt_f32_f16_e32 v84, v21
	s_waitcnt lgkmcnt(1)
	v_pk_fma_f32 v[22:23], v[86:87], v[54:55], v[22:23] op_sel_hi:[0,1,1]
	v_pk_fma_f32 v[30:31], v[86:87], v[54:55], v[30:31] op_sel:[1,0,0]
	v_pk_fma_f32 v[38:39], v[88:89], v[54:55], v[38:39] op_sel_hi:[0,1,1]
	v_pk_fma_f32 v[46:47], v[88:89], v[54:55], v[46:47] op_sel:[1,0,0]
	v_pk_fma_f32 v[24:25], v[86:87], v[56:57], v[24:25] op_sel_hi:[0,1,1]
	v_pk_fma_f32 v[32:33], v[86:87], v[56:57], v[32:33] op_sel:[1,0,0]
	v_pk_fma_f32 v[40:41], v[88:89], v[56:57], v[40:41] op_sel_hi:[0,1,1]
	v_pk_fma_f32 v[48:49], v[88:89], v[56:57], v[48:49] op_sel:[1,0,0]
	v_pk_fma_f32 v[26:27], v[86:87], v[58:59], v[26:27] op_sel_hi:[0,1,1]
	v_pk_fma_f32 v[34:35], v[86:87], v[58:59], v[34:35] op_sel:[1,0,0]
	v_pk_fma_f32 v[42:43], v[88:89], v[58:59], v[42:43] op_sel_hi:[0,1,1]
	v_pk_fma_f32 v[50:51], v[88:89], v[58:59], v[50:51] op_sel:[1,0,0]
	v_pk_fma_f32 v[28:29], v[86:87], v[60:61], v[28:29] op_sel_hi:[0,1,1]
	v_pk_fma_f32 v[36:37], v[86:87], v[60:61], v[36:37] op_sel:[1,0,0]
	v_pk_fma_f32 v[44:45], v[88:89], v[60:61], v[44:45] op_sel_hi:[0,1,1]
	v_pk_fma_f32 v[52:53], v[88:89], v[60:61], v[52:53] op_sel:[1,0,0]
	ds_read_b128 v[86:89], v72 offset:32
	v_cvt_f32_f16_sdwa v55, v74 dst_sel:DWORD dst_unused:UNUSED_PAD src0_sel:WORD_1
	v_cvt_f32_f16_e32 v54, v74
	v_cvt_f32_f16_sdwa v57, v75 dst_sel:DWORD dst_unused:UNUSED_PAD src0_sel:WORD_1
	v_cvt_f32_f16_e32 v56, v75
	v_cvt_f32_f16_sdwa v59, v76 dst_sel:DWORD dst_unused:UNUSED_PAD src0_sel:WORD_1
	v_cvt_f32_f16_e32 v58, v76
	v_cvt_f32_f16_sdwa v61, v77 dst_sel:DWORD dst_unused:UNUSED_PAD src0_sel:WORD_1
	v_cvt_f32_f16_e32 v60, v77
	s_waitcnt lgkmcnt(1)
	v_pk_fma_f32 v[22:23], v[90:91], v[78:79], v[22:23] op_sel_hi:[0,1,1]
	v_pk_fma_f32 v[30:31], v[90:91], v[78:79], v[30:31] op_sel:[1,0,0]
	v_pk_fma_f32 v[38:39], v[92:93], v[78:79], v[38:39] op_sel_hi:[0,1,1]
	v_pk_fma_f32 v[46:47], v[92:93], v[78:79], v[46:47] op_sel:[1,0,0]
	v_pk_fma_f32 v[24:25], v[90:91], v[80:81], v[24:25] op_sel_hi:[0,1,1]
	v_pk_fma_f32 v[32:33], v[90:91], v[80:81], v[32:33] op_sel:[1,0,0]
	v_pk_fma_f32 v[40:41], v[92:93], v[80:81], v[40:41] op_sel_hi:[0,1,1]
	v_pk_fma_f32 v[48:49], v[92:93], v[80:81], v[48:49] op_sel:[1,0,0]
	v_pk_fma_f32 v[26:27], v[90:91], v[82:83], v[26:27] op_sel_hi:[0,1,1]
	v_pk_fma_f32 v[34:35], v[90:91], v[82:83], v[34:35] op_sel:[1,0,0]
	v_pk_fma_f32 v[42:43], v[92:93], v[82:83], v[42:43] op_sel_hi:[0,1,1]
	v_pk_fma_f32 v[50:51], v[92:93], v[82:83], v[50:51] op_sel:[1,0,0]
	v_pk_fma_f32 v[28:29], v[90:91], v[84:85], v[28:29] op_sel_hi:[0,1,1]
	v_pk_fma_f32 v[36:37], v[90:91], v[84:85], v[36:37] op_sel:[1,0,0]
	v_pk_fma_f32 v[44:45], v[92:93], v[84:85], v[44:45] op_sel_hi:[0,1,1]
	v_pk_fma_f32 v[52:53], v[92:93], v[84:85], v[52:53] op_sel:[1,0,0]
	s_waitcnt lgkmcnt(0)
	v_pk_fma_f32 v[22:23], v[86:87], v[54:55], v[22:23] op_sel_hi:[0,1,1]
	v_pk_fma_f32 v[30:31], v[86:87], v[54:55], v[30:31] op_sel:[1,0,0]
	v_pk_fma_f32 v[38:39], v[88:89], v[54:55], v[38:39] op_sel_hi:[0,1,1]
	v_pk_fma_f32 v[46:47], v[88:89], v[54:55], v[46:47] op_sel:[1,0,0]
	v_pk_fma_f32 v[24:25], v[86:87], v[56:57], v[24:25] op_sel_hi:[0,1,1]
	v_pk_fma_f32 v[32:33], v[86:87], v[56:57], v[32:33] op_sel:[1,0,0]
	v_pk_fma_f32 v[40:41], v[88:89], v[56:57], v[40:41] op_sel_hi:[0,1,1]
	v_pk_fma_f32 v[48:49], v[88:89], v[56:57], v[48:49] op_sel:[1,0,0]
	v_pk_fma_f32 v[26:27], v[86:87], v[58:59], v[26:27] op_sel_hi:[0,1,1]
	v_pk_fma_f32 v[34:35], v[86:87], v[58:59], v[34:35] op_sel:[1,0,0]
	v_pk_fma_f32 v[42:43], v[88:89], v[58:59], v[42:43] op_sel_hi:[0,1,1]
	v_pk_fma_f32 v[50:51], v[88:89], v[58:59], v[50:51] op_sel:[1,0,0]
	v_pk_fma_f32 v[28:29], v[86:87], v[60:61], v[28:29] op_sel_hi:[0,1,1]
	v_pk_fma_f32 v[36:37], v[86:87], v[60:61], v[36:37] op_sel:[1,0,0]
	v_pk_fma_f32 v[44:45], v[88:89], v[60:61], v[44:45] op_sel_hi:[0,1,1]
	v_pk_fma_f32 v[52:53], v[88:89], v[60:61], v[52:53] op_sel:[1,0,0]
	s_branch .Ll1g_done
.Ll1g_lastE:
	ds_read_b128 v[86:89], v72
	ds_read_b128 v[90:93], v72 offset:16
	s_waitcnt vmcnt(0)
	v_cvt_f32_f16_sdwa v55, v2 dst_sel:DWORD dst_unused:UNUSED_PAD src0_sel:WORD_1
	v_cvt_f32_f16_e32 v54, v2
	v_cvt_f32_f16_sdwa v57, v3 dst_sel:DWORD dst_unused:UNUSED_PAD src0_sel:WORD_1
	v_cvt_f32_f16_e32 v56, v3
	v_cvt_f32_f16_sdwa v59, v4 dst_sel:DWORD dst_unused:UNUSED_PAD src0_sel:WORD_1
	v_cvt_f32_f16_e32 v58, v4
	v_cvt_f32_f16_sdwa v61, v5 dst_sel:DWORD dst_unused:UNUSED_PAD src0_sel:WORD_1
	v_cvt_f32_f16_e32 v60, v5
	v_cvt_f32_f16_sdwa v79, v6 dst_sel:DWORD dst_unused:UNUSED_PAD src0_sel:WORD_1
	v_cvt_f32_f16_e32 v78, v6
	v_cvt_f32_f16_sdwa v81, v7 dst_sel:DWORD dst_unused:UNUSED_PAD src0_sel:WORD_1
	v_cvt_f32_f16_e32 v80, v7
	v_cvt_f32_f16_sdwa v83, v8 dst_sel:DWORD dst_unused:UNUSED_PAD src0_sel:WORD_1
	v_cvt_f32_f16_e32 v82, v8
	v_cvt_f32_f16_sdwa v85, v9 dst_sel:DWORD dst_unused:UNUSED_PAD src0_sel:WORD_1
	v_cvt_f32_f16_e32 v84, v9
	s_waitcnt lgkmcnt(1)
	v_pk_fma_f32 v[22:23], v[86:87], v[54:55], v[22:23] op_sel_hi:[0,1,1]
	v_pk_fma_f32 v[30:31], v[86:87], v[54:55], v[30:31] op_sel:[1,0,0]
	v_pk_fma_f32 v[38:39], v[88:89], v[54:55], v[38:39] op_sel_hi:[0,1,1]
	v_pk_fma_f32 v[46:47], v[88:89], v[54:55], v[46:47] op_sel:[1,0,0]
	v_pk_fma_f32 v[24:25], v[86:87], v[56:57], v[24:25] op_sel_hi:[0,1,1]
	v_pk_fma_f32 v[32:33], v[86:87], v[56:57], v[32:33] op_sel:[1,0,0]
	v_pk_fma_f32 v[40:41], v[88:89], v[56:57], v[40:41] op_sel_hi:[0,1,1]
	v_pk_fma_f32 v[48:49], v[88:89], v[56:57], v[48:49] op_sel:[1,0,0]
	v_pk_fma_f32 v[26:27], v[86:87], v[58:59], v[26:27] op_sel_hi:[0,1,1]
	v_pk_fma_f32 v[34:35], v[86:87], v[58:59], v[34:35] op_sel:[1,0,0]
	v_pk_fma_f32 v[42:43], v[88:89], v[58:59], v[42:43] op_sel_hi:[0,1,1]
	v_pk_fma_f32 v[50:51], v[88:89], v[58:59], v[50:51] op_sel:[1,0,0]
	v_pk_fma_f32 v[28:29], v[86:87], v[60:61], v[28:29] op_sel_hi:[0,1,1]
	v_pk_fma_f32 v[36:37], v[86:87], v[60:61], v[36:37] op_sel:[1,0,0]
	v_pk_fma_f32 v[44:45], v[88:89], v[60:61], v[44:45] op_sel_hi:[0,1,1]
	v_pk_fma_f32 v[52:53], v[88:89], v[60:61], v[52:53] op_sel:[1,0,0]
	ds_read_b128 v[86:89], v72 offset:32
	v_cvt_f32_f16_sdwa v55, v10 dst_sel:DWORD dst_unused:UNUSED_PAD src0_sel:WORD_1
	v_cvt_f32_f16_e32 v54, v10
	v_cvt_f32_f16_sdwa v57, v11 dst_sel:DWORD dst_unused:UNUSED_PAD src0_sel:WORD_1
	v_cvt_f32_f16_e32 v56, v11
	v_cvt_f32_f16_sdwa v59, v12 dst_sel:DWORD dst_unused:UNUSED_PAD src0_sel:WORD_1
	v_cvt_f32_f16_e32 v58, v12
	v_cvt_f32_f16_sdwa v61, v13 dst_sel:DWORD dst_unused:UNUSED_PAD src0_sel:WORD_1
	v_cvt_f32_f16_e32 v60, v13
	s_waitcnt lgkmcnt(1)
	v_pk_fma_f32 v[22:23], v[90:91], v[78:79], v[22:23] op_sel_hi:[0,1,1]
	v_pk_fma_f32 v[30:31], v[90:91], v[78:79], v[30:31] op_sel:[1,0,0]
	v_pk_fma_f32 v[38:39], v[92:93], v[78:79], v[38:39] op_sel_hi:[0,1,1]
	v_pk_fma_f32 v[46:47], v[92:93], v[78:79], v[46:47] op_sel:[1,0,0]
	v_pk_fma_f32 v[24:25], v[90:91], v[80:81], v[24:25] op_sel_hi:[0,1,1]
	v_pk_fma_f32 v[32:33], v[90:91], v[80:81], v[32:33] op_sel:[1,0,0]
	v_pk_fma_f32 v[40:41], v[92:93], v[80:81], v[40:41] op_sel_hi:[0,1,1]
	v_pk_fma_f32 v[48:49], v[92:93], v[80:81], v[48:49] op_sel:[1,0,0]
	v_pk_fma_f32 v[26:27], v[90:91], v[82:83], v[26:27] op_sel_hi:[0,1,1]
	v_pk_fma_f32 v[34:35], v[90:91], v[82:83], v[34:35] op_sel:[1,0,0]
	v_pk_fma_f32 v[42:43], v[92:93], v[82:83], v[42:43] op_sel_hi:[0,1,1]
	v_pk_fma_f32 v[50:51], v[92:93], v[82:83], v[50:51] op_sel:[1,0,0]
	v_pk_fma_f32 v[28:29], v[90:91], v[84:85], v[28:29] op_sel_hi:[0,1,1]
	v_pk_fma_f32 v[36:37], v[90:91], v[84:85], v[36:37] op_sel:[1,0,0]
	v_pk_fma_f32 v[44:45], v[92:93], v[84:85], v[44:45] op_sel_hi:[0,1,1]
	v_pk_fma_f32 v[52:53], v[92:93], v[84:85], v[52:53] op_sel:[1,0,0]
	s_waitcnt lgkmcnt(0)
	v_pk_fma_f32 v[22:23], v[86:87], v[54:55], v[22:23] op_sel_hi:[0,1,1]
	v_pk_fma_f32 v[30:31], v[86:87], v[54:55], v[30:31] op_sel:[1,0,0]
	v_pk_fma_f32 v[38:39], v[88:89], v[54:55], v[38:39] op_sel_hi:[0,1,1]
	v_pk_fma_f32 v[46:47], v[88:89], v[54:55], v[46:47] op_sel:[1,0,0]
	v_pk_fma_f32 v[24:25], v[86:87], v[56:57], v[24:25] op_sel_hi:[0,1,1]
	v_pk_fma_f32 v[32:33], v[86:87], v[56:57], v[32:33] op_sel:[1,0,0]
	v_pk_fma_f32 v[40:41], v[88:89], v[56:57], v[40:41] op_sel_hi:[0,1,1]
	v_pk_fma_f32 v[48:49], v[88:89], v[56:57], v[48:49] op_sel:[1,0,0]
	v_pk_fma_f32 v[26:27], v[86:87], v[58:59], v[26:27] op_sel_hi:[0,1,1]
	v_pk_fma_f32 v[34:35], v[86:87], v[58:59], v[34:35] op_sel:[1,0,0]
	v_pk_fma_f32 v[42:43], v[88:89], v[58:59], v[42:43] op_sel_hi:[0,1,1]
	v_pk_fma_f32 v[50:51], v[88:89], v[58:59], v[50:51] op_sel:[1,0,0]
	v_pk_fma_f32 v[28:29], v[86:87], v[60:61], v[28:29] op_sel_hi:[0,1,1]
	v_pk_fma_f32 v[36:37], v[86:87], v[60:61], v[36:37] op_sel:[1,0,0]
	v_pk_fma_f32 v[44:45], v[88:89], v[60:61], v[44:45] op_sel_hi:[0,1,1]
	v_pk_fma_f32 v[52:53], v[88:89], v[60:61], v[52:53] op_sel:[1,0,0]
	s_branch .Ll1g_done
.Ll1g_tailO:
	s_add_i32 s5, s2, 3
	s_cmp_ge_i32 s5, s3
	s_cbranch_scc1 .Ll1g_lastO
	ds_read_b128 v[86:89], v72
	ds_read_b128 v[90:93], v72 offset:16
	s_waitcnt vmcnt(3)
	v_cvt_f32_f16_sdwa v55, v14 dst_sel:DWORD dst_unused:UNUSED_PAD src0_sel:WORD_1
	v_cvt_f32_f16_e32 v54, v14
	v_cvt_f32_f16_sdwa v57, v15 dst_sel:DWORD dst_unused:UNUSED_PAD src0_sel:WORD_1
	v_cvt_f32_f16_e32 v56, v15
	v_cvt_f32_f16_sdwa v59, v16 dst_sel:DWORD dst_unused:UNUSED_PAD src0_sel:WORD_1
	v_cvt_f32_f16_e32 v58, v16
	v_cvt_f32_f16_sdwa v61, v17 dst_sel:DWORD dst_unused:UNUSED_PAD src0_sel:WORD_1
	v_cvt_f32_f16_e32 v60, v17
	v_cvt_f32_f16_sdwa v79, v18 dst_sel:DWORD dst_unused:UNUSED_PAD src0_sel:WORD_1
	v_cvt_f32_f16_e32 v78, v18
	v_cvt_f32_f16_sdwa v81, v19 dst_sel:DWORD dst_unused:UNUSED_PAD src0_sel:WORD_1
	v_cvt_f32_f16_e32 v80, v19
	v_cvt_f32_f16_sdwa v83, v20 dst_sel:DWORD dst_unused:UNUSED_PAD src0_sel:WORD_1
	v_cvt_f32_f16_e32 v82, v20
	v_cvt_f32_f16_sdwa v85, v21 dst_sel:DWORD dst_unused:UNUSED_PAD src0_sel:WORD_1
	v_cvt_f32_f16_e32 v84, v21
	s_waitcnt lgkmcnt(1)
	v_pk_fma_f32 v[22:23], v[86:87], v[54:55], v[22:23] op_sel_hi:[0,1,1]
	v_pk_fma_f32 v[30:31], v[86:87], v[54:55], v[30:31] op_sel:[1,0,0]
	v_pk_fma_f32 v[38:39], v[88:89], v[54:55], v[38:39] op_sel_hi:[0,1,1]
	v_pk_fma_f32 v[46:47], v[88:89], v[54:55], v[46:47] op_sel:[1,0,0]
	v_pk_fma_f32 v[24:25], v[86:87], v[56:57], v[24:25] op_sel_hi:[0,1,1]
	v_pk_fma_f32 v[32:33], v[86:87], v[56:57], v[32:33] op_sel:[1,0,0]
	v_pk_fma_f32 v[40:41], v[88:89], v[56:57], v[40:41] op_sel_hi:[0,1,1]
	v_pk_fma_f32 v[48:49], v[88:89], v[56:57], v[48:49] op_sel:[1,0,0]
	v_pk_fma_f32 v[26:27], v[86:87], v[58:59], v[26:27] op_sel_hi:[0,1,1]
	v_pk_fma_f32 v[34:35], v[86:87], v[58:59], v[34:35] op_sel:[1,0,0]
	v_pk_fma_f32 v[42:43], v[88:89], v[58:59], v[42:43] op_sel_hi:[0,1,1]
	v_pk_fma_f32 v[50:51], v[88:89], v[58:59], v[50:51] op_sel:[1,0,0]
	v_pk_fma_f32 v[28:29], v[86:87], v[60:61], v[28:29] op_sel_hi:[0,1,1]
	v_pk_fma_f32 v[36:37], v[86:87], v[60:61], v[36:37] op_sel:[1,0,0]
	v_pk_fma_f32 v[44:45], v[88:89], v[60:61], v[44:45] op_sel_hi:[0,1,1]
	v_pk_fma_f32 v[52:53], v[88:89], v[60:61], v[52:53] op_sel:[1,0,0]
	ds_read_b128 v[86:89], v72 offset:32
	v_cvt_f32_f16_sdwa v55, v74 dst_sel:DWORD dst_unused:UNUSED_PAD src0_sel:WORD_1
	v_cvt_f32_f16_e32 v54, v74
	v_cvt_f32_f16_sdwa v57, v75 dst_sel:DWORD dst_unused:UNUSED_PAD src0_sel:WORD_1
	v_cvt_f32_f16_e32 v56, v75
	v_cvt_f32_f16_sdwa v59, v76 dst_sel:DWORD dst_unused:UNUSED_PAD src0_sel:WORD_1
	v_cvt_f32_f16_e32 v58, v76
	v_cvt_f32_f16_sdwa v61, v77 dst_sel:DWORD dst_unused:UNUSED_PAD src0_sel:WORD_1
	v_cvt_f32_f16_e32 v60, v77
	s_waitcnt lgkmcnt(1)
	v_pk_fma_f32 v[22:23], v[90:91], v[78:79], v[22:23] op_sel_hi:[0,1,1]
	v_pk_fma_f32 v[30:31], v[90:91], v[78:79], v[30:31] op_sel:[1,0,0]
	v_pk_fma_f32 v[38:39], v[92:93], v[78:79], v[38:39] op_sel_hi:[0,1,1]
	v_pk_fma_f32 v[46:47], v[92:93], v[78:79], v[46:47] op_sel:[1,0,0]
	v_pk_fma_f32 v[24:25], v[90:91], v[80:81], v[24:25] op_sel_hi:[0,1,1]
	v_pk_fma_f32 v[32:33], v[90:91], v[80:81], v[32:33] op_sel:[1,0,0]
	v_pk_fma_f32 v[40:41], v[92:93], v[80:81], v[40:41] op_sel_hi:[0,1,1]
	v_pk_fma_f32 v[48:49], v[92:93], v[80:81], v[48:49] op_sel:[1,0,0]
	v_pk_fma_f32 v[26:27], v[90:91], v[82:83], v[26:27] op_sel_hi:[0,1,1]
	v_pk_fma_f32 v[34:35], v[90:91], v[82:83], v[34:35] op_sel:[1,0,0]
	v_pk_fma_f32 v[42:43], v[92:93], v[82:83], v[42:43] op_sel_hi:[0,1,1]
	v_pk_fma_f32 v[50:51], v[92:93], v[82:83], v[50:51] op_sel:[1,0,0]
	v_pk_fma_f32 v[28:29], v[90:91], v[84:85], v[28:29] op_sel_hi:[0,1,1]
	v_pk_fma_f32 v[36:37], v[90:91], v[84:85], v[36:37] op_sel:[1,0,0]
	v_pk_fma_f32 v[44:45], v[92:93], v[84:85], v[44:45] op_sel_hi:[0,1,1]
	v_pk_fma_f32 v[52:53], v[92:93], v[84:85], v[52:53] op_sel:[1,0,0]
	s_waitcnt lgkmcnt(0)
	v_pk_fma_f32 v[22:23], v[86:87], v[54:55], v[22:23] op_sel_hi:[0,1,1]
	v_pk_fma_f32 v[30:31], v[86:87], v[54:55], v[30:31] op_sel:[1,0,0]
	v_pk_fma_f32 v[38:39], v[88:89], v[54:55], v[38:39] op_sel_hi:[0,1,1]
	v_pk_fma_f32 v[46:47], v[88:89], v[54:55], v[46:47] op_sel:[1,0,0]
	v_pk_fma_f32 v[24:25], v[86:87], v[56:57], v[24:25] op_sel_hi:[0,1,1]
	v_pk_fma_f32 v[32:33], v[86:87], v[56:57], v[32:33] op_sel:[1,0,0]
	v_pk_fma_f32 v[40:41], v[88:89], v[56:57], v[40:41] op_sel_hi:[0,1,1]
	v_pk_fma_f32 v[48:49], v[88:89], v[56:57], v[48:49] op_sel:[1,0,0]
	v_pk_fma_f32 v[26:27], v[86:87], v[58:59], v[26:27] op_sel_hi:[0,1,1]
	v_pk_fma_f32 v[34:35], v[86:87], v[58:59], v[34:35] op_sel:[1,0,0]
	v_pk_fma_f32 v[42:43], v[88:89], v[58:59], v[42:43] op_sel_hi:[0,1,1]
	v_pk_fma_f32 v[50:51], v[88:89], v[58:59], v[50:51] op_sel:[1,0,0]
	v_pk_fma_f32 v[28:29], v[86:87], v[60:61], v[28:29] op_sel_hi:[0,1,1]
	v_pk_fma_f32 v[36:37], v[86:87], v[60:61], v[36:37] op_sel:[1,0,0]
	v_pk_fma_f32 v[44:45], v[88:89], v[60:61], v[44:45] op_sel_hi:[0,1,1]
	v_pk_fma_f32 v[52:53], v[88:89], v[60:61], v[52:53] op_sel:[1,0,0]
	v_add_u32_e32 v72, 48, v72
	s_add_i32 s2, s2, 3
	ds_read_b128 v[86:89], v72
	ds_read_b128 v[90:93], v72 offset:16
	s_waitcnt vmcnt(0)
	v_cvt_f32_f16_sdwa v55, v2 dst_sel:DWORD dst_unused:UNUSED_PAD src0_sel:WORD_1
	v_cvt_f32_f16_e32 v54, v2
	v_cvt_f32_f16_sdwa v57, v3 dst_sel:DWORD dst_unused:UNUSED_PAD src0_sel:WORD_1
	v_cvt_f32_f16_e32 v56, v3
	v_cvt_f32_f16_sdwa v59, v4 dst_sel:DWORD dst_unused:UNUSED_PAD src0_sel:WORD_1
	v_cvt_f32_f16_e32 v58, v4
	v_cvt_f32_f16_sdwa v61, v5 dst_sel:DWORD dst_unused:UNUSED_PAD src0_sel:WORD_1
	v_cvt_f32_f16_e32 v60, v5
	v_cvt_f32_f16_sdwa v79, v6 dst_sel:DWORD dst_unused:UNUSED_PAD src0_sel:WORD_1
	v_cvt_f32_f16_e32 v78, v6
	v_cvt_f32_f16_sdwa v81, v7 dst_sel:DWORD dst_unused:UNUSED_PAD src0_sel:WORD_1
	v_cvt_f32_f16_e32 v80, v7
	v_cvt_f32_f16_sdwa v83, v8 dst_sel:DWORD dst_unused:UNUSED_PAD src0_sel:WORD_1
	v_cvt_f32_f16_e32 v82, v8
	v_cvt_f32_f16_sdwa v85, v9 dst_sel:DWORD dst_unused:UNUSED_PAD src0_sel:WORD_1
	v_cvt_f32_f16_e32 v84, v9
	s_waitcnt lgkmcnt(1)
	v_pk_fma_f32 v[22:23], v[86:87], v[54:55], v[22:23] op_sel_hi:[0,1,1]
	v_pk_fma_f32 v[30:31], v[86:87], v[54:55], v[30:31] op_sel:[1,0,0]
	v_pk_fma_f32 v[38:39], v[88:89], v[54:55], v[38:39] op_sel_hi:[0,1,1]
	v_pk_fma_f32 v[46:47], v[88:89], v[54:55], v[46:47] op_sel:[1,0,0]
	v_pk_fma_f32 v[24:25], v[86:87], v[56:57], v[24:25] op_sel_hi:[0,1,1]
	v_pk_fma_f32 v[32:33], v[86:87], v[56:57], v[32:33] op_sel:[1,0,0]
	v_pk_fma_f32 v[40:41], v[88:89], v[56:57], v[40:41] op_sel_hi:[0,1,1]
	v_pk_fma_f32 v[48:49], v[88:89], v[56:57], v[48:49] op_sel:[1,0,0]
	v_pk_fma_f32 v[26:27], v[86:87], v[58:59], v[26:27] op_sel_hi:[0,1,1]
	v_pk_fma_f32 v[34:35], v[86:87], v[58:59], v[34:35] op_sel:[1,0,0]
	v_pk_fma_f32 v[42:43], v[88:89], v[58:59], v[42:43] op_sel_hi:[0,1,1]
	v_pk_fma_f32 v[50:51], v[88:89], v[58:59], v[50:51] op_sel:[1,0,0]
	v_pk_fma_f32 v[28:29], v[86:87], v[60:61], v[28:29] op_sel_hi:[0,1,1]
	v_pk_fma_f32 v[36:37], v[86:87], v[60:61], v[36:37] op_sel:[1,0,0]
	v_pk_fma_f32 v[44:45], v[88:89], v[60:61], v[44:45] op_sel_hi:[0,1,1]
	v_pk_fma_f32 v[52:53], v[88:89], v[60:61], v[52:53] op_sel:[1,0,0]
	ds_read_b128 v[86:89], v72 offset:32
	v_cvt_f32_f16_sdwa v55, v10 dst_sel:DWORD dst_unused:UNUSED_PAD src0_sel:WORD_1
	v_cvt_f32_f16_e32 v54, v10
	v_cvt_f32_f16_sdwa v57, v11 dst_sel:DWORD dst_unused:UNUSED_PAD src0_sel:WORD_1
	v_cvt_f32_f16_e32 v56, v11
	v_cvt_f32_f16_sdwa v59, v12 dst_sel:DWORD dst_unused:UNUSED_PAD src0_sel:WORD_1
	v_cvt_f32_f16_e32 v58, v12
	v_cvt_f32_f16_sdwa v61, v13 dst_sel:DWORD dst_unused:UNUSED_PAD src0_sel:WORD_1
	v_cvt_f32_f16_e32 v60, v13
	s_waitcnt lgkmcnt(1)
	v_pk_fma_f32 v[22:23], v[90:91], v[78:79], v[22:23] op_sel_hi:[0,1,1]
	v_pk_fma_f32 v[30:31], v[90:91], v[78:79], v[30:31] op_sel:[1,0,0]
	v_pk_fma_f32 v[38:39], v[92:93], v[78:79], v[38:39] op_sel_hi:[0,1,1]
	v_pk_fma_f32 v[46:47], v[92:93], v[78:79], v[46:47] op_sel:[1,0,0]
	v_pk_fma_f32 v[24:25], v[90:91], v[80:81], v[24:25] op_sel_hi:[0,1,1]
	v_pk_fma_f32 v[32:33], v[90:91], v[80:81], v[32:33] op_sel:[1,0,0]
	v_pk_fma_f32 v[40:41], v[92:93], v[80:81], v[40:41] op_sel_hi:[0,1,1]
	v_pk_fma_f32 v[48:49], v[92:93], v[80:81], v[48:49] op_sel:[1,0,0]
	v_pk_fma_f32 v[26:27], v[90:91], v[82:83], v[26:27] op_sel_hi:[0,1,1]
	v_pk_fma_f32 v[34:35], v[90:91], v[82:83], v[34:35] op_sel:[1,0,0]
	v_pk_fma_f32 v[42:43], v[92:93], v[82:83], v[42:43] op_sel_hi:[0,1,1]
	v_pk_fma_f32 v[50:51], v[92:93], v[82:83], v[50:51] op_sel:[1,0,0]
	v_pk_fma_f32 v[28:29], v[90:91], v[84:85], v[28:29] op_sel_hi:[0,1,1]
	v_pk_fma_f32 v[36:37], v[90:91], v[84:85], v[36:37] op_sel:[1,0,0]
	v_pk_fma_f32 v[44:45], v[92:93], v[84:85], v[44:45] op_sel_hi:[0,1,1]
	v_pk_fma_f32 v[52:53], v[92:93], v[84:85], v[52:53] op_sel:[1,0,0]
	s_waitcnt lgkmcnt(0)
	v_pk_fma_f32 v[22:23], v[86:87], v[54:55], v[22:23] op_sel_hi:[0,1,1]
	v_pk_fma_f32 v[30:31], v[86:87], v[54:55], v[30:31] op_sel:[1,0,0]
	v_pk_fma_f32 v[38:39], v[88:89], v[54:55], v[38:39] op_sel_hi:[0,1,1]
	v_pk_fma_f32 v[46:47], v[88:89], v[54:55], v[46:47] op_sel:[1,0,0]
	v_pk_fma_f32 v[24:25], v[86:87], v[56:57], v[24:25] op_sel_hi:[0,1,1]
	v_pk_fma_f32 v[32:33], v[86:87], v[56:57], v[32:33] op_sel:[1,0,0]
	v_pk_fma_f32 v[40:41], v[88:89], v[56:57], v[40:41] op_sel_hi:[0,1,1]
	v_pk_fma_f32 v[48:49], v[88:89], v[56:57], v[48:49] op_sel:[1,0,0]
	v_pk_fma_f32 v[26:27], v[86:87], v[58:59], v[26:27] op_sel_hi:[0,1,1]
	v_pk_fma_f32 v[34:35], v[86:87], v[58:59], v[34:35] op_sel:[1,0,0]
	v_pk_fma_f32 v[42:43], v[88:89], v[58:59], v[42:43] op_sel_hi:[0,1,1]
	v_pk_fma_f32 v[50:51], v[88:89], v[58:59], v[50:51] op_sel:[1,0,0]
	v_pk_fma_f32 v[28:29], v[86:87], v[60:61], v[28:29] op_sel_hi:[0,1,1]
	v_pk_fma_f32 v[36:37], v[86:87], v[60:61], v[36:37] op_sel:[1,0,0]
	v_pk_fma_f32 v[44:45], v[88:89], v[60:61], v[44:45] op_sel_hi:[0,1,1]
	v_pk_fma_f32 v[52:53], v[88:89], v[60:61], v[52:53] op_sel:[1,0,0]
	s_branch .Ll1g_done
.Ll1g_lastO:
	ds_read_b128 v[86:89], v72
	ds_read_b128 v[90:93], v72 offset:16
	s_waitcnt vmcnt(0)
	v_cvt_f32_f16_sdwa v55, v14 dst_sel:DWORD dst_unused:UNUSED_PAD src0_sel:WORD_1
	v_cvt_f32_f16_e32 v54, v14
	v_cvt_f32_f16_sdwa v57, v15 dst_sel:DWORD dst_unused:UNUSED_PAD src0_sel:WORD_1
	v_cvt_f32_f16_e32 v56, v15
	v_cvt_f32_f16_sdwa v59, v16 dst_sel:DWORD dst_unused:UNUSED_PAD src0_sel:WORD_1
	v_cvt_f32_f16_e32 v58, v16
	v_cvt_f32_f16_sdwa v61, v17 dst_sel:DWORD dst_unused:UNUSED_PAD src0_sel:WORD_1
	v_cvt_f32_f16_e32 v60, v17
	v_cvt_f32_f16_sdwa v79, v18 dst_sel:DWORD dst_unused:UNUSED_PAD src0_sel:WORD_1
	v_cvt_f32_f16_e32 v78, v18
	v_cvt_f32_f16_sdwa v81, v19 dst_sel:DWORD dst_unused:UNUSED_PAD src0_sel:WORD_1
	v_cvt_f32_f16_e32 v80, v19
	v_cvt_f32_f16_sdwa v83, v20 dst_sel:DWORD dst_unused:UNUSED_PAD src0_sel:WORD_1
	v_cvt_f32_f16_e32 v82, v20
	v_cvt_f32_f16_sdwa v85, v21 dst_sel:DWORD dst_unused:UNUSED_PAD src0_sel:WORD_1
	v_cvt_f32_f16_e32 v84, v21
	s_waitcnt lgkmcnt(1)
	v_pk_fma_f32 v[22:23], v[86:87], v[54:55], v[22:23] op_sel_hi:[0,1,1]
	v_pk_fma_f32 v[30:31], v[86:87], v[54:55], v[30:31] op_sel:[1,0,0]
	v_pk_fma_f32 v[38:39], v[88:89], v[54:55], v[38:39] op_sel_hi:[0,1,1]
	v_pk_fma_f32 v[46:47], v[88:89], v[54:55], v[46:47] op_sel:[1,0,0]
	v_pk_fma_f32 v[24:25], v[86:87], v[56:57], v[24:25] op_sel_hi:[0,1,1]
	v_pk_fma_f32 v[32:33], v[86:87], v[56:57], v[32:33] op_sel:[1,0,0]
	v_pk_fma_f32 v[40:41], v[88:89], v[56:57], v[40:41] op_sel_hi:[0,1,1]
	v_pk_fma_f32 v[48:49], v[88:89], v[56:57], v[48:49] op_sel:[1,0,0]
	v_pk_fma_f32 v[26:27], v[86:87], v[58:59], v[26:27] op_sel_hi:[0,1,1]
	v_pk_fma_f32 v[34:35], v[86:87], v[58:59], v[34:35] op_sel:[1,0,0]
	v_pk_fma_f32 v[42:43], v[88:89], v[58:59], v[42:43] op_sel_hi:[0,1,1]
	v_pk_fma_f32 v[50:51], v[88:89], v[58:59], v[50:51] op_sel:[1,0,0]
	v_pk_fma_f32 v[28:29], v[86:87], v[60:61], v[28:29] op_sel_hi:[0,1,1]
	v_pk_fma_f32 v[36:37], v[86:87], v[60:61], v[36:37] op_sel:[1,0,0]
	v_pk_fma_f32 v[44:45], v[88:89], v[60:61], v[44:45] op_sel_hi:[0,1,1]
	v_pk_fma_f32 v[52:53], v[88:89], v[60:61], v[52:53] op_sel:[1,0,0]
	ds_read_b128 v[86:89], v72 offset:32
	v_cvt_f32_f16_sdwa v55, v74 dst_sel:DWORD dst_unused:UNUSED_PAD src0_sel:WORD_1
	v_cvt_f32_f16_e32 v54, v74
	v_cvt_f32_f16_sdwa v57, v75 dst_sel:DWORD dst_unused:UNUSED_PAD src0_sel:WORD_1
	v_cvt_f32_f16_e32 v56, v75
	v_cvt_f32_f16_sdwa v59, v76 dst_sel:DWORD dst_unused:UNUSED_PAD src0_sel:WORD_1
	v_cvt_f32_f16_e32 v58, v76
	v_cvt_f32_f16_sdwa v61, v77 dst_sel:DWORD dst_unused:UNUSED_PAD src0_sel:WORD_1
	v_cvt_f32_f16_e32 v60, v77
	s_waitcnt lgkmcnt(1)
	v_pk_fma_f32 v[22:23], v[90:91], v[78:79], v[22:23] op_sel_hi:[0,1,1]
	v_pk_fma_f32 v[30:31], v[90:91], v[78:79], v[30:31] op_sel:[1,0,0]
	v_pk_fma_f32 v[38:39], v[92:93], v[78:79], v[38:39] op_sel_hi:[0,1,1]
	v_pk_fma_f32 v[46:47], v[92:93], v[78:79], v[46:47] op_sel:[1,0,0]
	v_pk_fma_f32 v[24:25], v[90:91], v[80:81], v[24:25] op_sel_hi:[0,1,1]
	v_pk_fma_f32 v[32:33], v[90:91], v[80:81], v[32:33] op_sel:[1,0,0]
	v_pk_fma_f32 v[40:41], v[92:93], v[80:81], v[40:41] op_sel_hi:[0,1,1]
	v_pk_fma_f32 v[48:49], v[92:93], v[80:81], v[48:49] op_sel:[1,0,0]
	v_pk_fma_f32 v[26:27], v[90:91], v[82:83], v[26:27] op_sel_hi:[0,1,1]
	v_pk_fma_f32 v[34:35], v[90:91], v[82:83], v[34:35] op_sel:[1,0,0]
	v_pk_fma_f32 v[42:43], v[92:93], v[82:83], v[42:43] op_sel_hi:[0,1,1]
	v_pk_fma_f32 v[50:51], v[92:93], v[82:83], v[50:51] op_sel:[1,0,0]
	v_pk_fma_f32 v[28:29], v[90:91], v[84:85], v[28:29] op_sel_hi:[0,1,1]
	v_pk_fma_f32 v[36:37], v[90:91], v[84:85], v[36:37] op_sel:[1,0,0]
	v_pk_fma_f32 v[44:45], v[92:93], v[84:85], v[44:45] op_sel_hi:[0,1,1]
	v_pk_fma_f32 v[52:53], v[92:93], v[84:85], v[52:53] op_sel:[1,0,0]
	s_waitcnt lgkmcnt(0)
	v_pk_fma_f32 v[22:23], v[86:87], v[54:55], v[22:23] op_sel_hi:[0,1,1]
	v_pk_fma_f32 v[30:31], v[86:87], v[54:55], v[30:31] op_sel:[1,0,0]
	v_pk_fma_f32 v[38:39], v[88:89], v[54:55], v[38:39] op_sel_hi:[0,1,1]
	v_pk_fma_f32 v[46:47], v[88:89], v[54:55], v[46:47] op_sel:[1,0,0]
	v_pk_fma_f32 v[24:25], v[86:87], v[56:57], v[24:25] op_sel_hi:[0,1,1]
	v_pk_fma_f32 v[32:33], v[86:87], v[56:57], v[32:33] op_sel:[1,0,0]
	v_pk_fma_f32 v[40:41], v[88:89], v[56:57], v[40:41] op_sel_hi:[0,1,1]
	v_pk_fma_f32 v[48:49], v[88:89], v[56:57], v[48:49] op_sel:[1,0,0]
	v_pk_fma_f32 v[26:27], v[86:87], v[58:59], v[26:27] op_sel_hi:[0,1,1]
	v_pk_fma_f32 v[34:35], v[86:87], v[58:59], v[34:35] op_sel:[1,0,0]
	v_pk_fma_f32 v[42:43], v[88:89], v[58:59], v[42:43] op_sel_hi:[0,1,1]
	v_pk_fma_f32 v[50:51], v[88:89], v[58:59], v[50:51] op_sel:[1,0,0]
	v_pk_fma_f32 v[28:29], v[86:87], v[60:61], v[28:29] op_sel_hi:[0,1,1]
	v_pk_fma_f32 v[36:37], v[86:87], v[60:61], v[36:37] op_sel:[1,0,0]
	v_pk_fma_f32 v[44:45], v[88:89], v[60:61], v[44:45] op_sel_hi:[0,1,1]
	v_pk_fma_f32 v[52:53], v[88:89], v[60:61], v[52:53] op_sel:[1,0,0]
.Ll1g_done:
	s_setprio 0
	v_add_u32_e32 v6, v70, v71
	v_cvt_pk_f16_f32 v2, v22, v23
	v_cvt_pk_f16_f32 v3, v24, v25
	v_cvt_pk_f16_f32 v4, v26, v27
	v_cvt_pk_f16_f32 v5, v28, v29
	ds_write_b128 v6, v[2:5]
	v_cvt_pk_f16_f32 v2, v30, v31
	v_cvt_pk_f16_f32 v3, v32, v33
	v_cvt_pk_f16_f32 v4, v34, v35
	v_cvt_pk_f16_f32 v5, v36, v37
	ds_write_b128 v6, v[2:5] offset:256
	v_cvt_pk_f16_f32 v2, v38, v39
	v_cvt_pk_f16_f32 v3, v40, v41
	v_cvt_pk_f16_f32 v4, v42, v43
	v_cvt_pk_f16_f32 v5, v44, v45
	ds_write_b128 v6, v[2:5] offset:512
	v_cvt_pk_f16_f32 v2, v46, v47
	v_cvt_pk_f16_f32 v3, v48, v49
	v_cvt_pk_f16_f32 v4, v50, v51
	v_cvt_pk_f16_f32 v5, v52, v53
	ds_write_b128 v6, v[2:5] offset:768

.LBB2_57:
	s_endpgm
	s_nop 0
	s_nop 0
	s_nop 0
	s_nop 0
	s_nop 0
	s_nop 0
	s_nop 0
	s_nop 0
	s_nop 0
	s_nop 0
	s_nop 0
	s_nop 0
	s_nop 0
	s_nop 0
	s_nop 0
	s_nop 0
	s_nop 0
	s_nop 0
	s_nop 0
	s_nop 0
	s_nop 0
	s_nop 0
	s_nop 0
	s_nop 0
	s_nop 0
	s_nop 0
	s_nop 0
	s_nop 0
	s_nop 0
	s_nop 0
	s_nop 0
	s_nop 0
	s_nop 0
	s_nop 0
	s_nop 0
	s_nop 0
	s_endpgm

	.amdhsa_kernel _ZN12_GLOBAL__N_18k_layer1EPKDF16_PKfS3_PKiPK15HIP_vector_typeIjLj4EES1_S3_S1_S3_S3_PDF16_PfSB_S3_
		.amdhsa_group_segment_fixed_size 25216
		.amdhsa_private_segment_fixed_size 0
		.amdhsa_kernarg_size 112
		.amdhsa_user_sgpr_count 2
		.amdhsa_user_sgpr_dispatch_ptr 0
		.amdhsa_user_sgpr_queue_ptr 0
		.amdhsa_user_sgpr_kernarg_segment_ptr 1
		.amdhsa_user_sgpr_dispatch_id 0
		.amdhsa_user_sgpr_kernarg_preload_length 0
		.amdhsa_user_sgpr_kernarg_preload_offset 0
		.amdhsa_user_sgpr_private_segment_size 0
		.amdhsa_uses_dynamic_stack 0
		.amdhsa_enable_private_segment 0
		.amdhsa_system_sgpr_workgroup_id_x 1
		.amdhsa_system_sgpr_workgroup_id_y 0
		.amdhsa_system_sgpr_workgroup_id_z 0
		.amdhsa_system_sgpr_workgroup_info 0
		.amdhsa_system_vgpr_workitem_id 0
		.amdhsa_next_free_vgpr 96
		.amdhsa_next_free_sgpr 100
		.amdhsa_accum_offset 96
		.amdhsa_reserve_vcc 1
		.amdhsa_float_round_mode_32 0
		.amdhsa_float_round_mode_16_64 0
		.amdhsa_float_denorm_mode_32 3
		.amdhsa_float_denorm_mode_16_64 3
		.amdhsa_dx10_clamp 1
		.amdhsa_ieee_mode 1
		.amdhsa_fp16_overflow 0
		.amdhsa_tg_split 0
		.amdhsa_exception_fp_ieee_invalid_op 0
		.amdhsa_exception_fp_denorm_src 0
		.amdhsa_exception_fp_ieee_div_zero 0
		.amdhsa_exception_fp_ieee_overflow 0
		.amdhsa_exception_fp_ieee_underflow 0
		.amdhsa_exception_fp_ieee_inexact 0
		.amdhsa_exception_int_div_zero 0
	.end_amdhsa_kernel

amdhsa.kernels:
  - .agpr_count:     0
    .args:
      - .actual_access:  read_only
        .address_space:  global
        .offset:         0
        .size:           8
        .value_kind:     global_buffer
      - .actual_access:  read_only
        .address_space:  global
        .offset:         8
        .size:           8
        .value_kind:     global_buffer
      - .actual_access:  read_only
        .address_space:  global
        .offset:         16
        .size:           8
        .value_kind:     global_buffer
      - .actual_access:  read_only
        .address_space:  global
        .offset:         24
        .size:           8
        .value_kind:     global_buffer
      - .actual_access:  read_only
        .address_space:  global
        .offset:         32
        .size:           8
        .value_kind:     global_buffer
      - .actual_access:  read_only
        .address_space:  global
        .offset:         40
        .size:           8
        .value_kind:     global_buffer
      - .actual_access:  read_only
        .address_space:  global
        .offset:         48
        .size:           8
        .value_kind:     global_buffer
      - .actual_access:  read_only
        .address_space:  global
        .offset:         56
        .size:           8
        .value_kind:     global_buffer
      - .actual_access:  read_only
        .address_space:  global
        .offset:         64
        .size:           8
        .value_kind:     global_buffer
      - .actual_access:  read_only
        .address_space:  global
        .offset:         72
        .size:           8
        .value_kind:     global_buffer
      - .actual_access:  read_only
        .address_space:  global
        .offset:         80
        .size:           8
        .value_kind:     global_buffer
      - .actual_access:  read_only
        .address_space:  global
        .offset:         88
        .size:           8
        .value_kind:     global_buffer
      - .actual_access:  write_only
        .address_space:  global
        .offset:         96
        .size:           8
        .value_kind:     global_buffer
      - .actual_access:  write_only
        .address_space:  global
        .offset:         104
        .size:           8
        .value_kind:     global_buffer
      - .actual_access:  write_only
        .address_space:  global
        .offset:         112
        .size:           8
        .value_kind:     global_buffer
      - .actual_access:  write_only
        .address_space:  global
        .offset:         120
        .size:           8
        .value_kind:     global_buffer
      - .actual_access:  write_only
        .address_space:  global
        .offset:         128
        .size:           8
        .value_kind:     global_buffer
      - .actual_access:  write_only
        .address_space:  global
        .offset:         136
        .size:           8
        .value_kind:     global_buffer
      - .actual_access:  read_only
        .address_space:  global
        .offset:         144
        .size:           8
        .value_kind:     global_buffer
      - .actual_access:  read_only
        .address_space:  global
        .offset:         152
        .size:           8
        .value_kind:     global_buffer
      - .actual_access:  read_only
        .address_space:  global
        .offset:         160
        .size:           8
        .value_kind:     global_buffer
      - .actual_access:  write_only
        .address_space:  global
        .offset:         168
        .size:           8
        .value_kind:     global_buffer
    .group_segment_fixed_size: 4272
    .kernarg_segment_align: 8
    .kernarg_segment_size: 176
    .language:       OpenCL C
    .language_version:
      - 2
      - 0
    .max_flat_workgroup_size: 256
    .name:           _ZN12_GLOBAL__N_16k_prepEPKfPKiS1_S1_S1_S1_S1_S1_S1_S1_S1_S1_P15HIP_vector_typeIjLj4EEPiPfPDF16_S9_S9_S1_S1_S1_S8_
    .private_segment_fixed_size: 0
    .sgpr_count:     30
    .sgpr_spill_count: 0
    .symbol:         _ZN12_GLOBAL__N_16k_prepEPKfPKiS1_S1_S1_S1_S1_S1_S1_S1_S1_S1_P15HIP_vector_typeIjLj4EEPiPfPDF16_S9_S9_S1_S1_S1_S8_.kd
    .uniform_work_group_size: 1
    .uses_dynamic_stack: false
    .vgpr_count:     144
    .vgpr_spill_count: 0
    .wavefront_size: 64
  - .agpr_count:     0
    .args:
      - .actual_access:  read_only
        .address_space:  global
        .offset:         0
        .size:           8
        .value_kind:     global_buffer
      - .actual_access:  read_only
        .address_space:  global
        .offset:         8
        .size:           8
        .value_kind:     global_buffer
      - .actual_access:  write_only
        .address_space:  global
        .offset:         16
        .size:           8
        .value_kind:     global_buffer
      - .actual_access:  write_only
        .address_space:  global
        .offset:         24
        .size:           8
        .value_kind:     global_buffer
      - .actual_access:  read_only
        .address_space:  global
        .offset:         32
        .size:           8
        .value_kind:     global_buffer
      - .actual_access:  read_only
        .address_space:  global
        .offset:         40
        .size:           8
        .value_kind:     global_buffer
      - .actual_access:  write_only
        .address_space:  global
        .offset:         48
        .size:           8
        .value_kind:     global_buffer
      - .actual_access:  write_only
        .address_space:  global
        .offset:         56
        .size:           8
        .value_kind:     global_buffer
      - .actual_access:  write_only
        .address_space:  global
        .offset:         64
        .size:           8
        .value_kind:     global_buffer
    .group_segment_fixed_size: 7268
    .kernarg_segment_align: 8
    .kernarg_segment_size: 72
    .language:       OpenCL C
    .language_version:
      - 2
      - 0
    .max_flat_workgroup_size: 1024
    .name:           _ZN12_GLOBAL__N_18k_bucketEPK15HIP_vector_typeIjLj4EEPKiPiPS1_PKfS9_PDF16_PfSB_
    .private_segment_fixed_size: 0
    .sgpr_count:     26
    .sgpr_spill_count: 0
    .symbol:         _ZN12_GLOBAL__N_18k_bucketEPK15HIP_vector_typeIjLj4EEPKiPiPS1_PKfS9_PDF16_PfSB_.kd
    .uniform_work_group_size: 1
    .uses_dynamic_stack: false
    .vgpr_count:     62
    .vgpr_spill_count: 0
    .wavefront_size: 64
  - .agpr_count:     0
    .args:
      - .actual_access:  read_only
        .address_space:  global
        .offset:         0
        .size:           8
        .value_kind:     global_buffer
      - .actual_access:  read_only
        .address_space:  global
        .offset:         8
        .size:           8
        .value_kind:     global_buffer
      - .actual_access:  read_only
        .address_space:  global
        .offset:         16
        .size:           8
        .value_kind:     global_buffer
      - .actual_access:  read_only
        .address_space:  global
        .offset:         24
        .size:           8
        .value_kind:     global_buffer
      - .actual_access:  read_only
        .address_space:  global
        .offset:         32
        .size:           8
        .value_kind:     global_buffer
      - .actual_access:  read_only
        .address_space:  global
        .offset:         40
        .size:           8
        .value_kind:     global_buffer
      - .actual_access:  read_only
        .address_space:  global
        .offset:         48
        .size:           8
        .value_kind:     global_buffer
      - .actual_access:  read_only
        .address_space:  global
        .offset:         56
        .size:           8
        .value_kind:     global_buffer
      - .actual_access:  read_only
        .address_space:  global
        .offset:         64
        .size:           8
        .value_kind:     global_buffer
      - .actual_access:  read_only
        .address_space:  global
        .offset:         72
        .size:           8
        .value_kind:     global_buffer
      - .actual_access:  write_only
        .address_space:  global
        .offset:         80
        .size:           8
        .value_kind:     global_buffer
      - .actual_access:  write_only
        .address_space:  global
        .offset:         88
        .size:           8
        .value_kind:     global_buffer
      - .actual_access:  write_only
        .address_space:  global
        .offset:         96
        .size:           8
        .value_kind:     global_buffer
      - .actual_access:  read_only
        .address_space:  global
        .offset:         104
        .size:           8
        .value_kind:     global_buffer
    .group_segment_fixed_size: 25216
    .kernarg_segment_align: 8
    .kernarg_segment_size: 112
    .language:       OpenCL C
    .language_version:
      - 2
      - 0
    .max_flat_workgroup_size: 256
    .name:           _ZN12_GLOBAL__N_18k_layer1EPKDF16_PKfS3_PKiPK15HIP_vector_typeIjLj4EES1_S3_S1_S3_S3_PDF16_PfSB_S3_
    .private_segment_fixed_size: 0
    .sgpr_count:     106
    .sgpr_spill_count: 0
    .symbol:         _ZN12_GLOBAL__N_18k_layer1EPKDF16_PKfS3_PKiPK15HIP_vector_typeIjLj4EES1_S3_S1_S3_S3_PDF16_PfSB_S3_.kd
    .uniform_work_group_size: 1
    .uses_dynamic_stack: false
    .vgpr_count:     96
    .vgpr_spill_count: 0
    .wavefront_size: 64
  - .agpr_count:     0
    .args:
      - .actual_access:  read_only
        .address_space:  global
        .offset:         0
        .size:           8
        .value_kind:     global_buffer
      - .actual_access:  read_only
        .address_space:  global
        .offset:         8
        .size:           8
        .value_kind:     global_buffer
      - .actual_access:  read_only
        .address_space:  global
        .offset:         16
        .size:           8
        .value_kind:     global_buffer
      - .actual_access:  read_only
        .address_space:  global
        .offset:         24
        .size:           8
        .value_kind:     global_buffer
      - .actual_access:  read_only
        .address_space:  global
        .offset:         32
        .size:           8
        .value_kind:     global_buffer
      - .actual_access:  read_only
        .address_space:  global
        .offset:         40
        .size:           8
        .value_kind:     global_buffer
      - .actual_access:  read_only
        .address_space:  global
        .offset:         48
        .size:           8
        .value_kind:     global_buffer
      - .actual_access:  write_only
        .address_space:  global
        .offset:         56
        .size:           8
        .value_kind:     global_buffer
    .group_segment_fixed_size: 6144
    .kernarg_segment_align: 8
    .kernarg_segment_size: 64
    .language:       OpenCL C
    .language_version:
      - 2
      - 0
    .max_flat_workgroup_size: 256
    .name:           _ZN12_GLOBAL__N_18k_layer2EPKDF16_PKfS3_PKiPK15HIP_vector_typeIjLj4EES3_S3_PDF16_
    .private_segment_fixed_size: 0
    .sgpr_count:     42
    .sgpr_spill_count: 0
    .symbol:         _ZN12_GLOBAL__N_18k_layer2EPKDF16_PKfS3_PKiPK15HIP_vector_typeIjLj4EES3_S3_PDF16_.kd
    .uniform_work_group_size: 1
    .uses_dynamic_stack: false
    .vgpr_count:     70
    .vgpr_spill_count: 0
    .wavefront_size: 64
  - .agpr_count:     0
    .args:
      - .actual_access:  read_only
        .address_space:  global
        .offset:         0
        .size:           8
        .value_kind:     global_buffer
      - .actual_access:  read_only
        .address_space:  global
        .offset:         8
        .size:           8
        .value_kind:     global_buffer
      - .actual_access:  read_only
        .address_space:  global
        .offset:         16
        .size:           8
        .value_kind:     global_buffer
      - .actual_access:  read_only
        .address_space:  global
        .offset:         24
        .size:           8
        .value_kind:     global_buffer
      - .actual_access:  read_only
        .address_space:  global
        .offset:         32
        .size:           8
        .value_kind:     global_buffer
      - .actual_access:  read_only
        .address_space:  global
        .offset:         40
        .size:           8
        .value_kind:     global_buffer
      - .actual_access:  write_only
        .address_space:  global
        .offset:         48
        .size:           8
        .value_kind:     global_buffer
    .group_segment_fixed_size: 16384
    .kernarg_segment_align: 8
    .kernarg_segment_size: 56
    .language:       OpenCL C
    .language_version:
      - 2
      - 0
    .max_flat_workgroup_size: 512
    .name:           _ZN12_GLOBAL__N_17k_pairsEPKDF16_PKiS1_PKfS5_S5_Pf
    .private_segment_fixed_size: 0
    .sgpr_count:     18
    .sgpr_spill_count: 0
    .symbol:         _ZN12_GLOBAL__N_17k_pairsEPKDF16_PKiS1_PKfS5_S5_Pf.kd
    .uniform_work_group_size: 1
    .uses_dynamic_stack: false
    .vgpr_count:     59
    .vgpr_spill_count: 0
    .wavefront_size: 64
